# P9 gate-row pointer walks as a 32-bit offset from the array base (31 64-bit adds -> 32-bit adds, SGPR-base loads), on top of v100
# speedup vs baseline: 1.0034x; 1.0034x over previous
.LBB0_1503:
	s_or_b64 exec, exec, s[48:49]
	s_ashr_i32 s45, s44, 31
	v_readlane_b32 s43, v254, 9
	s_ashr_i32 s47, s46, 31
	s_add_i32 s53, s53, s43
	s_lshl_b64 s[44:45], s[44:45], 7
	s_lshl_b64 s[46:47], s[46:47], 17
	s_add_u32 s46, s31, s46
	s_addc_u32 s47, s33, s47
	ds_write_b128 v173, v[22:25]
	s_waitcnt lgkmcnt(0)
	ds_write_b128 v174, v[2:5]
	ds_write_b128 v175, v[6:9]
	ds_write_b128 v176, v[10:13]
	ds_write_b128 v177, v[14:17] offset:128
	ds_write_b128 v178, v[18:21] offset:128
	ds_write_b128 v179, v[26:29] offset:128
	ds_write_b128 v180, v[30:33] offset:128
	ds_write_b128 v181, v[34:37] offset:256
	ds_write_b128 v182, v[38:41] offset:256
	ds_write_b128 v183, v[42:45] offset:256
	ds_write_b128 v184, v[46:49] offset:256
	ds_write_b128 v185, v[50:53] offset:384
	ds_write_b128 v186, v[54:57] offset:384
	ds_write_b128 v187, v[58:61] offset:384
	ds_write_b128 v188, v[62:65] offset:384
	global_load_dwordx4 v[22:25], v66, s[46:47] nt
	global_load_dwordx4 v[2:5], v66, s[46:47] offset:1024 nt
	global_load_dwordx4 v[6:9], v66, s[46:47] offset:2048 nt
	s_nop 0
	global_load_dwordx4 v[10:13], v66, s[46:47] offset:3072 nt
	s_nop 0
	global_load_dwordx4 v[14:17], v74, s[46:47] nt
	s_nop 0
	global_load_dwordx4 v[18:21], v76, s[46:47] nt
	s_nop 0
	global_load_dwordx4 v[26:29], v78, s[46:47] nt
	s_nop 0
	global_load_dwordx4 v[30:33], v80, s[46:47] nt
	s_nop 0
	global_load_dwordx4 v[34:37], v82, s[46:47] nt
	s_nop 0
	global_load_dwordx4 v[38:41], v84, s[46:47] nt
	s_nop 0
	global_load_dwordx4 v[42:45], v86, s[46:47] nt
	s_nop 0
	global_load_dwordx4 v[46:49], v88, s[46:47] nt
	ds_read2_b64 v[60:63], v189 offset1:16
	s_waitcnt lgkmcnt(14)
	v_pk_fma_f32 v[148:149], v[148:149], 0, v[152:153] op_sel_hi:[1,0,1]
	v_pk_fma_f32 v[144:145], v[148:149], v[144:145], v[150:151]
	s_waitcnt lgkmcnt(0)
	v_lshlrev_b32_e32 v64, 16, v60
	v_pk_fma_f32 v[140:141], v[144:145], v[140:141], v[146:147]
	v_lshlrev_b32_e32 v65, 16, v61
	v_add_f32_e32 v144, 0, v64
	v_pk_fma_f32 v[138:139], v[140:141], v[138:139], v[142:143]
	v_exp_f32_e32 v142, v64
	v_add_f32_e32 v145, 0, v65
	v_exp_f32_e32 v143, v65
	v_lshlrev_b32_e32 v64, 16, v62
	v_lshlrev_b32_e32 v65, 16, v63
	global_load_dwordx4 v[50:53], v90, s[46:47] nt
	s_nop 0
	global_load_dwordx4 v[54:57], v92, s[46:47] nt
	v_add_f32_e32 v148, v144, v64
	v_add_f32_e32 v149, v145, v65
	ds_read2_b64 v[144:147], v189 offset0:32 offset1:48
	v_exp_f32_e32 v64, v64
	v_exp_f32_e32 v65, v65
	v_and_b32_e32 v141, 0xffff0000, v60
	v_fma_f32 v60, 0, v142, v141
	v_and_b32_e32 v140, 0xffff0000, v61
	v_and_b32_e32 v62, 0xffff0000, v62
	v_fma_f32 v61, 0, v143, v140
	v_fmac_f32_e32 v62, v64, v60
	v_and_b32_e32 v60, 0xffff0000, v63
	s_waitcnt lgkmcnt(0)
	v_lshlrev_b32_e32 v63, 16, v145
	v_fmac_f32_e32 v60, v65, v61
	v_lshlrev_b32_e32 v61, 16, v144
	v_add_f32_e32 v65, v149, v63
	v_add_f32_e32 v64, v148, v61
	v_exp_f32_e32 v63, v63
	v_exp_f32_e32 v61, v61
	v_and_b32_e32 v145, 0xffff0000, v145
	v_and_b32_e32 v144, 0xffff0000, v144
	v_fmac_f32_e32 v145, v63, v60
	v_lshlrev_b32_e32 v60, 16, v146
	v_fmac_f32_e32 v144, v61, v62
	v_lshlrev_b32_e32 v61, 16, v147
	v_add_f32_e32 v64, v64, v60
	v_exp_f32_e32 v148, v60
	v_add_f32_e32 v65, v65, v61
	v_exp_f32_e32 v149, v61
	ds_read2_b64 v[60:63], v189 offset0:64 offset1:80
	v_and_b32_e32 v146, 0xffff0000, v146
	v_fmac_f32_e32 v146, v148, v144
	v_and_b32_e32 v144, 0xffff0000, v147
	v_fmac_f32_e32 v144, v149, v145
	s_waitcnt lgkmcnt(0)
	v_lshlrev_b32_e32 v147, 16, v61
	v_lshlrev_b32_e32 v145, 16, v60
	v_add_f32_e32 v65, v65, v147
	v_add_f32_e32 v64, v64, v145
	v_exp_f32_e32 v147, v147
	v_exp_f32_e32 v145, v145
	v_and_b32_e32 v61, 0xffff0000, v61
	v_and_b32_e32 v60, 0xffff0000, v60
	v_fmac_f32_e32 v61, v147, v144
	v_lshlrev_b32_e32 v144, 16, v62
	v_fmac_f32_e32 v60, v145, v146
	v_lshlrev_b32_e32 v145, 16, v63
	v_add_f32_e32 v64, v64, v144
	v_exp_f32_e32 v148, v144
	v_add_f32_e32 v65, v65, v145
	v_exp_f32_e32 v149, v145
	ds_read2_b64 v[144:147], v189 offset0:96 offset1:112
	v_and_b32_e32 v62, 0xffff0000, v62
	v_fmac_f32_e32 v62, v148, v60
	v_and_b32_e32 v60, 0xffff0000, v63
	v_fmac_f32_e32 v60, v149, v61
	s_waitcnt lgkmcnt(0)
	v_lshlrev_b32_e32 v63, 16, v145
	v_lshlrev_b32_e32 v61, 16, v144
	v_add_f32_e32 v65, v65, v63
	v_add_f32_e32 v64, v64, v61
	v_exp_f32_e32 v63, v63
	v_exp_f32_e32 v61, v61
	v_and_b32_e32 v145, 0xffff0000, v145
	v_and_b32_e32 v144, 0xffff0000, v144
	v_fmac_f32_e32 v145, v63, v60
	v_lshlrev_b32_e32 v60, 16, v146
	v_fmac_f32_e32 v144, v61, v62
	v_lshlrev_b32_e32 v61, 16, v147
	v_add_f32_e32 v64, v64, v60
	v_exp_f32_e32 v148, v60
	v_add_f32_e32 v65, v65, v61
	v_exp_f32_e32 v149, v61
	ds_read2_b64 v[60:63], v189 offset0:128 offset1:144
	v_and_b32_e32 v146, 0xffff0000, v146
	v_fmac_f32_e32 v146, v148, v144
	v_and_b32_e32 v144, 0xffff0000, v147
	v_fmac_f32_e32 v144, v149, v145
	s_waitcnt lgkmcnt(0)
	v_lshlrev_b32_e32 v147, 16, v61
	v_lshlrev_b32_e32 v145, 16, v60
	v_add_f32_e32 v65, v65, v147
	v_add_f32_e32 v64, v64, v145
	v_exp_f32_e32 v147, v147
	v_exp_f32_e32 v145, v145
	v_and_b32_e32 v61, 0xffff0000, v61
	v_and_b32_e32 v60, 0xffff0000, v60
	v_fmac_f32_e32 v61, v147, v144
	v_lshlrev_b32_e32 v144, 16, v62
	v_fmac_f32_e32 v60, v145, v146
	v_lshlrev_b32_e32 v145, 16, v63
	v_add_f32_e32 v64, v64, v144
	v_exp_f32_e32 v148, v144
	v_add_f32_e32 v65, v65, v145
	v_exp_f32_e32 v149, v145
	ds_read2_b64 v[144:147], v189 offset0:160 offset1:176
	v_and_b32_e32 v62, 0xffff0000, v62
	v_fmac_f32_e32 v62, v148, v60
	v_and_b32_e32 v60, 0xffff0000, v63
	v_fmac_f32_e32 v60, v149, v61
	s_waitcnt lgkmcnt(0)
	v_lshlrev_b32_e32 v63, 16, v145
	v_lshlrev_b32_e32 v61, 16, v144
	v_add_f32_e32 v65, v65, v63
	v_add_f32_e32 v64, v64, v61
	v_exp_f32_e32 v63, v63
	v_exp_f32_e32 v61, v61
	v_and_b32_e32 v145, 0xffff0000, v145
	v_and_b32_e32 v144, 0xffff0000, v144
	v_fmac_f32_e32 v145, v63, v60
	v_lshlrev_b32_e32 v60, 16, v146
	v_fmac_f32_e32 v144, v61, v62
	v_lshlrev_b32_e32 v61, 16, v147
	v_add_f32_e32 v64, v64, v60
	v_exp_f32_e32 v148, v60
	v_add_f32_e32 v65, v65, v61
	v_exp_f32_e32 v149, v61
	ds_read2_b64 v[60:63], v189 offset0:192 offset1:208
	v_and_b32_e32 v146, 0xffff0000, v146
	v_fmac_f32_e32 v146, v148, v144
	v_and_b32_e32 v144, 0xffff0000, v147
	v_fmac_f32_e32 v144, v149, v145
	s_waitcnt lgkmcnt(0)
	v_lshlrev_b32_e32 v147, 16, v61
	v_lshlrev_b32_e32 v145, 16, v60
	v_add_f32_e32 v65, v65, v147
	v_add_f32_e32 v64, v64, v145
	v_exp_f32_e32 v147, v147
	v_exp_f32_e32 v145, v145
	v_and_b32_e32 v61, 0xffff0000, v61
	v_and_b32_e32 v60, 0xffff0000, v60
	v_fmac_f32_e32 v61, v147, v144
	v_lshlrev_b32_e32 v144, 16, v62
	v_fmac_f32_e32 v60, v145, v146
	v_lshlrev_b32_e32 v145, 16, v63
	v_add_f32_e32 v64, v64, v144
	v_exp_f32_e32 v148, v144
	v_add_f32_e32 v65, v65, v145
	v_exp_f32_e32 v149, v145
	ds_read2_b64 v[144:147], v189 offset0:224 offset1:240
	v_and_b32_e32 v62, 0xffff0000, v62
	v_fmac_f32_e32 v62, v148, v60
	v_and_b32_e32 v60, 0xffff0000, v63
	v_fmac_f32_e32 v60, v149, v61
	s_waitcnt lgkmcnt(0)
	v_lshlrev_b32_e32 v63, 16, v145
	v_lshlrev_b32_e32 v61, 16, v144
	v_add_f32_e32 v65, v65, v63
	v_add_f32_e32 v64, v64, v61
	v_exp_f32_e32 v63, v63
	v_exp_f32_e32 v61, v61
	v_and_b32_e32 v145, 0xffff0000, v145
	v_and_b32_e32 v144, 0xffff0000, v144
	v_fmac_f32_e32 v145, v63, v60
	v_lshlrev_b32_e32 v60, 16, v146
	v_fmac_f32_e32 v144, v61, v62
	v_lshlrev_b32_e32 v61, 16, v147
	v_add_f32_e32 v64, v64, v60
	v_exp_f32_e32 v148, v60
	v_add_u32_e32 v150, 0x800, v189
	v_add_f32_e32 v65, v65, v61
	v_exp_f32_e32 v149, v61
	ds_read2_b64 v[60:63], v150 offset1:16
	v_and_b32_e32 v146, 0xffff0000, v146
	v_fmac_f32_e32 v146, v148, v144
	v_and_b32_e32 v144, 0xffff0000, v147
	v_fmac_f32_e32 v144, v149, v145
	s_waitcnt lgkmcnt(0)
	v_lshlrev_b32_e32 v147, 16, v61
	v_lshlrev_b32_e32 v145, 16, v60
	v_add_f32_e32 v65, v65, v147
	v_add_f32_e32 v64, v64, v145
	v_exp_f32_e32 v147, v147
	v_exp_f32_e32 v145, v145
	v_and_b32_e32 v61, 0xffff0000, v61
	v_and_b32_e32 v60, 0xffff0000, v60
	v_fmac_f32_e32 v61, v147, v144
	v_lshlrev_b32_e32 v144, 16, v62
	v_fmac_f32_e32 v60, v145, v146
	v_lshlrev_b32_e32 v145, 16, v63
	v_add_f32_e32 v64, v64, v144
	v_exp_f32_e32 v148, v144
	v_add_f32_e32 v65, v65, v145
	v_exp_f32_e32 v149, v145
	ds_read2_b64 v[144:147], v150 offset0:32 offset1:48
	v_and_b32_e32 v62, 0xffff0000, v62
	v_fmac_f32_e32 v62, v148, v60
	v_and_b32_e32 v60, 0xffff0000, v63
	v_fmac_f32_e32 v60, v149, v61
	s_waitcnt lgkmcnt(0)
	v_lshlrev_b32_e32 v63, 16, v145
	v_lshlrev_b32_e32 v61, 16, v144
	v_add_f32_e32 v65, v65, v63
	v_add_f32_e32 v64, v64, v61
	v_exp_f32_e32 v63, v63
	v_exp_f32_e32 v61, v61
	v_and_b32_e32 v145, 0xffff0000, v145
	v_and_b32_e32 v144, 0xffff0000, v144
	v_fmac_f32_e32 v145, v63, v60
	v_lshlrev_b32_e32 v60, 16, v146
	v_fmac_f32_e32 v144, v61, v62
	v_lshlrev_b32_e32 v61, 16, v147
	v_add_f32_e32 v64, v64, v60
	v_exp_f32_e32 v148, v60
	v_add_f32_e32 v65, v65, v61
	v_exp_f32_e32 v149, v61
	ds_read2_b64 v[60:63], v150 offset0:64 offset1:80
	v_and_b32_e32 v146, 0xffff0000, v146
	v_fmac_f32_e32 v146, v148, v144
	v_and_b32_e32 v144, 0xffff0000, v147
	v_fmac_f32_e32 v144, v149, v145
	s_waitcnt lgkmcnt(0)
	v_lshlrev_b32_e32 v147, 16, v61
	v_lshlrev_b32_e32 v145, 16, v60
	v_add_f32_e32 v65, v65, v147
	v_add_f32_e32 v64, v64, v145
	v_exp_f32_e32 v147, v147
	v_exp_f32_e32 v145, v145
	v_and_b32_e32 v61, 0xffff0000, v61
	v_and_b32_e32 v60, 0xffff0000, v60
	v_fmac_f32_e32 v61, v147, v144
	v_lshlrev_b32_e32 v144, 16, v62
	v_fmac_f32_e32 v60, v145, v146
	v_lshlrev_b32_e32 v145, 16, v63
	v_add_f32_e32 v64, v64, v144
	v_exp_f32_e32 v148, v144
	v_add_f32_e32 v65, v65, v145
	v_exp_f32_e32 v149, v145
	ds_read2_b64 v[144:147], v150 offset0:96 offset1:112
	v_and_b32_e32 v62, 0xffff0000, v62
	v_fmac_f32_e32 v62, v148, v60
	v_and_b32_e32 v60, 0xffff0000, v63
	v_fmac_f32_e32 v60, v149, v61
	s_waitcnt lgkmcnt(0)
	v_lshlrev_b32_e32 v63, 16, v145
	v_lshlrev_b32_e32 v61, 16, v144
	v_add_f32_e32 v65, v65, v63
	v_add_f32_e32 v64, v64, v61
	v_exp_f32_e32 v63, v63
	v_exp_f32_e32 v61, v61
	v_and_b32_e32 v145, 0xffff0000, v145
	v_and_b32_e32 v144, 0xffff0000, v144
	v_fmac_f32_e32 v145, v63, v60
	v_lshlrev_b32_e32 v60, 16, v146
	v_fmac_f32_e32 v144, v61, v62
	v_lshlrev_b32_e32 v61, 16, v147
	v_add_f32_e32 v64, v64, v60
	v_exp_f32_e32 v148, v60
	v_add_f32_e32 v65, v65, v61
	v_exp_f32_e32 v149, v61
	ds_read2_b64 v[60:63], v150 offset0:128 offset1:144
	v_and_b32_e32 v146, 0xffff0000, v146
	v_fmac_f32_e32 v146, v148, v144
	v_and_b32_e32 v144, 0xffff0000, v147
	v_fmac_f32_e32 v144, v149, v145
	s_waitcnt lgkmcnt(0)
	v_lshlrev_b32_e32 v147, 16, v61
	v_lshlrev_b32_e32 v145, 16, v60
	v_add_f32_e32 v65, v65, v147
	v_add_f32_e32 v64, v64, v145
	v_exp_f32_e32 v147, v147
	v_exp_f32_e32 v145, v145
	v_and_b32_e32 v61, 0xffff0000, v61
	v_and_b32_e32 v60, 0xffff0000, v60
	v_fmac_f32_e32 v61, v147, v144
	v_lshlrev_b32_e32 v144, 16, v62
	v_fmac_f32_e32 v60, v145, v146
	v_lshlrev_b32_e32 v145, 16, v63
	v_add_f32_e32 v64, v64, v144
	v_exp_f32_e32 v148, v144
	v_add_f32_e32 v65, v65, v145
	v_exp_f32_e32 v149, v145
	ds_read2_b64 v[144:147], v150 offset0:160 offset1:176
	v_and_b32_e32 v62, 0xffff0000, v62
	v_fmac_f32_e32 v62, v148, v60
	v_and_b32_e32 v60, 0xffff0000, v63
	v_fmac_f32_e32 v60, v149, v61
	s_waitcnt lgkmcnt(0)
	v_lshlrev_b32_e32 v63, 16, v145
	v_lshlrev_b32_e32 v61, 16, v144
	v_add_f32_e32 v65, v65, v63
	v_add_f32_e32 v64, v64, v61
	v_exp_f32_e32 v63, v63
	v_exp_f32_e32 v61, v61
	v_and_b32_e32 v145, 0xffff0000, v145
	v_and_b32_e32 v144, 0xffff0000, v144
	v_fmac_f32_e32 v145, v63, v60
	v_lshlrev_b32_e32 v60, 16, v146
	v_fmac_f32_e32 v144, v61, v62
	v_lshlrev_b32_e32 v61, 16, v147
	v_add_f32_e32 v64, v64, v60
	v_exp_f32_e32 v148, v60
	v_add_f32_e32 v65, v65, v61
	v_exp_f32_e32 v149, v61
	ds_read2_b64 v[60:63], v150 offset0:192 offset1:208
	v_and_b32_e32 v146, 0xffff0000, v146
	v_fmac_f32_e32 v146, v148, v144
	v_and_b32_e32 v144, 0xffff0000, v147
	v_fmac_f32_e32 v144, v149, v145
	s_waitcnt lgkmcnt(0)
	v_lshlrev_b32_e32 v147, 16, v61
	v_lshlrev_b32_e32 v145, 16, v60
	v_add_f32_e32 v65, v65, v147
	v_add_f32_e32 v64, v64, v145
	v_exp_f32_e32 v147, v147
	v_exp_f32_e32 v145, v145
	v_and_b32_e32 v61, 0xffff0000, v61
	v_and_b32_e32 v60, 0xffff0000, v60
	v_fmac_f32_e32 v61, v147, v144
	v_lshlrev_b32_e32 v144, 16, v62
	v_fmac_f32_e32 v60, v145, v146
	v_lshlrev_b32_e32 v145, 16, v63
	v_add_f32_e32 v64, v64, v144
	v_exp_f32_e32 v148, v144
	v_add_f32_e32 v65, v65, v145
	v_exp_f32_e32 v149, v145
	ds_read2_b64 v[144:147], v150 offset0:224 offset1:240
	v_and_b32_e32 v62, 0xffff0000, v62
	v_fmac_f32_e32 v62, v148, v60
	v_and_b32_e32 v60, 0xffff0000, v63
	v_fmac_f32_e32 v60, v149, v61
	s_waitcnt lgkmcnt(0)
	v_lshlrev_b32_e32 v61, 16, v144
	v_lshlrev_b32_e32 v63, 16, v145
	v_add_f32_e32 v64, v64, v61
	v_add_f32_e32 v65, v65, v63
	v_exp_f32_e32 v61, v61
	v_exp_f32_e32 v63, v63
	v_and_b32_e32 v144, 0xffff0000, v144
	v_fmac_f32_e32 v144, v61, v62
	v_and_b32_e32 v61, 0xffff0000, v145
	v_fmac_f32_e32 v61, v63, v60
	v_lshlrev_b32_e32 v60, 16, v146
	v_exp_f32_e32 v63, v60
	v_lshlrev_b32_e32 v62, 16, v147
	v_add_f32_e32 v60, v64, v60
	v_add_f32_e32 v64, v65, v62
	v_and_b32_e32 v145, 0xffff0000, v146
	v_fmac_f32_e32 v145, v63, v144
	v_exp_f32_e32 v62, v62
	v_exp_f32_e32 v144, v60
	v_exp_f32_e32 v146, v64
	v_and_b32_e32 v147, 0xffff0000, v147
	v_fmac_f32_e32 v147, v62, v61
	ds_bpermute_b32 v148, v73, v144
	ds_bpermute_b32 v149, v73, v146
	ds_bpermute_b32 v150, v73, v145
	ds_bpermute_b32 v151, v73, v147
	global_load_dwordx4 v[58:61], v94, s[46:47] nt
	s_nop 0
	global_load_dwordx4 v[62:65], v96, s[46:47] nt
	s_waitcnt lgkmcnt(1)
	v_fmac_f32_e32 v150, v138, v148
	s_waitcnt lgkmcnt(0)
	v_fmac_f32_e32 v151, v139, v149
	ds_bpermute_b32 v148, v166, v144
	ds_bpermute_b32 v149, v166, v145
	v_cndmask_b32_e64 v139, v151, v139, s[0:1]
	v_cndmask_b32_e64 v138, v150, v138, s[0:1]
	ds_bpermute_b32 v150, v166, v146
	ds_bpermute_b32 v151, v166, v147
	ds_bpermute_b32 v144, v167, v144
	ds_bpermute_b32 v146, v167, v146
	ds_bpermute_b32 v145, v167, v145
	ds_bpermute_b32 v147, v167, v147
	s_waitcnt lgkmcnt(6)
	v_fmac_f32_e32 v149, v138, v148
	s_waitcnt lgkmcnt(4)
	v_fmac_f32_e32 v151, v139, v150
	v_cndmask_b32_e64 v139, v139, v151, s[4:5]
	v_cndmask_b32_e64 v138, v138, v149, s[4:5]
	s_waitcnt lgkmcnt(1)
	v_fmac_f32_e32 v145, v138, v144
	s_waitcnt lgkmcnt(0)
	v_fmac_f32_e32 v147, v139, v146
	v_cndmask_b32_e64 v139, v139, v147, s[6:7]
	v_cndmask_b32_e64 v138, v138, v145, s[6:7]
	v_fmac_f32_e32 v141, v142, v138
	v_fmac_f32_e32 v140, v143, v139
	v_cvt_pk_bf16_f32 v138, v141, v140
	ds_read_b64 v[142:143], v189 offset:128
	s_cmpk_gt_i32 s53, 0x27ff
	s_waitcnt lgkmcnt(0)
	v_lshlrev_b32_e32 v139, 16, v142
	v_lshlrev_b32_e32 v144, 16, v143
	v_exp_f32_e32 v139, v139
	v_exp_f32_e32 v144, v144
	v_and_b32_e32 v142, 0xffff0000, v142
	v_and_b32_e32 v143, 0xffff0000, v143
	v_fmac_f32_e32 v142, v141, v139
	v_fmac_f32_e32 v143, v140, v144
	v_cvt_pk_bf16_f32 v139, v142, v143
	ds_read_b64 v[140:141], v189 offset:256
	s_waitcnt lgkmcnt(0)
	v_lshlrev_b32_e32 v144, 16, v140
	v_lshlrev_b32_e32 v145, 16, v141
	v_exp_f32_e32 v144, v144
	v_exp_f32_e32 v145, v145
	v_and_b32_e32 v146, 0xffff0000, v140
	v_and_b32_e32 v141, 0xffff0000, v141
	v_fmac_f32_e32 v146, v142, v144
	v_fmac_f32_e32 v141, v143, v145
	v_cvt_pk_bf16_f32 v140, v146, v141
	ds_read_b64 v[142:143], v189 offset:384
	s_waitcnt lgkmcnt(0)
	v_lshlrev_b32_e32 v144, 16, v142
	v_lshlrev_b32_e32 v145, 16, v143
	v_exp_f32_e32 v144, v144
	v_exp_f32_e32 v145, v145
	v_and_b32_e32 v147, 0xffff0000, v142
	v_fmac_f32_e32 v147, v146, v144
	v_and_b32_e32 v144, 0xffff0000, v143
	v_fmac_f32_e32 v144, v141, v145
	v_cvt_pk_bf16_f32 v141, v147, v144
	ds_read_b64 v[142:143], v189 offset:512
	s_waitcnt lgkmcnt(0)
	v_lshlrev_b32_e32 v145, 16, v142
	v_lshlrev_b32_e32 v146, 16, v143
	v_exp_f32_e32 v145, v145
	v_exp_f32_e32 v146, v146
	v_and_b32_e32 v148, 0xffff0000, v142
	v_and_b32_e32 v143, 0xffff0000, v143
	v_fmac_f32_e32 v148, v147, v145
	v_fmac_f32_e32 v143, v144, v146
	v_cvt_pk_bf16_f32 v142, v148, v143
	ds_read_b64 v[144:145], v189 offset:640
	s_waitcnt lgkmcnt(0)
	v_lshlrev_b32_e32 v146, 16, v144
	v_lshlrev_b32_e32 v147, 16, v145
	v_exp_f32_e32 v146, v146
	v_exp_f32_e32 v147, v147
	v_and_b32_e32 v149, 0xffff0000, v144
	v_fmac_f32_e32 v149, v148, v146
	v_and_b32_e32 v146, 0xffff0000, v145
	v_fmac_f32_e32 v146, v143, v147
	v_cvt_pk_bf16_f32 v143, v149, v146
	ds_read_b64 v[144:145], v189 offset:768
	s_waitcnt lgkmcnt(0)
	v_lshlrev_b32_e32 v147, 16, v144
	v_lshlrev_b32_e32 v148, 16, v145
	v_exp_f32_e32 v147, v147
	v_exp_f32_e32 v148, v148
	v_and_b32_e32 v150, 0xffff0000, v144
	v_and_b32_e32 v145, 0xffff0000, v145
	v_fmac_f32_e32 v150, v149, v147
	v_fmac_f32_e32 v145, v146, v148
	v_cvt_pk_bf16_f32 v144, v150, v145
	ds_read_b64 v[146:147], v189 offset:896
	s_waitcnt lgkmcnt(0)
	v_lshlrev_b32_e32 v148, 16, v146
	v_lshlrev_b32_e32 v149, 16, v147
	v_exp_f32_e32 v148, v148
	v_exp_f32_e32 v149, v149
	v_and_b32_e32 v151, 0xffff0000, v146
	v_and_b32_e32 v147, 0xffff0000, v147
	v_fmac_f32_e32 v151, v150, v148
	v_fmac_f32_e32 v147, v145, v149
	v_cvt_pk_bf16_f32 v146, v151, v147
	ds_read_b64 v[148:149], v189 offset:1024
	s_waitcnt lgkmcnt(0)
	v_lshlrev_b32_e32 v145, 16, v148
	v_lshlrev_b32_e32 v150, 16, v149
	v_exp_f32_e32 v145, v145
	v_exp_f32_e32 v150, v150
	v_and_b32_e32 v152, 0xffff0000, v148
	v_fmac_f32_e32 v152, v151, v145
	v_and_b32_e32 v145, 0xffff0000, v149
	v_fmac_f32_e32 v145, v147, v150
	v_cvt_pk_bf16_f32 v148, v152, v145
	ds_read_b64 v[150:151], v189 offset:1152
	s_waitcnt lgkmcnt(0)
	v_lshlrev_b32_e32 v147, 16, v150
	v_lshlrev_b32_e32 v149, 16, v151
	v_exp_f32_e32 v147, v147
	v_exp_f32_e32 v149, v149
	v_and_b32_e32 v154, 0xffff0000, v150
	v_fmac_f32_e32 v154, v152, v147
	v_and_b32_e32 v147, 0xffff0000, v151
	v_fmac_f32_e32 v147, v145, v149
	v_cvt_pk_bf16_f32 v150, v154, v147
	ds_read_b64 v[152:153], v189 offset:1280
	s_waitcnt lgkmcnt(0)
	v_lshlrev_b32_e32 v145, 16, v152
	v_lshlrev_b32_e32 v149, 16, v153
	v_exp_f32_e32 v145, v145
	v_exp_f32_e32 v149, v149
	v_and_b32_e32 v151, 0xffff0000, v152
	v_fmac_f32_e32 v151, v154, v145
	v_and_b32_e32 v145, 0xffff0000, v153
	v_fmac_f32_e32 v145, v147, v149
	v_cvt_pk_bf16_f32 v152, v151, v145
	ds_read_b64 v[154:155], v189 offset:1408
	s_waitcnt lgkmcnt(0)
	v_lshlrev_b32_e32 v147, 16, v154
	v_lshlrev_b32_e32 v149, 16, v155
	v_exp_f32_e32 v147, v147
	v_exp_f32_e32 v149, v149
	v_and_b32_e32 v153, 0xffff0000, v154
	v_fmac_f32_e32 v153, v151, v147
	v_and_b32_e32 v147, 0xffff0000, v155
	v_fmac_f32_e32 v147, v145, v149
	v_cvt_pk_bf16_f32 v155, v153, v147
	ds_read_b64 v[156:157], v189 offset:1536
	s_waitcnt lgkmcnt(0)
	v_lshlrev_b32_e32 v145, 16, v156
	v_lshlrev_b32_e32 v149, 16, v157
	v_exp_f32_e32 v145, v145
	v_exp_f32_e32 v149, v149
	v_and_b32_e32 v151, 0xffff0000, v156
	v_fmac_f32_e32 v151, v153, v145
	v_and_b32_e32 v145, 0xffff0000, v157
	v_fmac_f32_e32 v145, v147, v149
	v_cvt_pk_bf16_f32 v157, v151, v145
	ds_read_b64 v[194:195], v189 offset:1664
	s_waitcnt lgkmcnt(0)
	v_lshlrev_b32_e32 v147, 16, v194
	v_lshlrev_b32_e32 v149, 16, v195
	v_exp_f32_e32 v147, v147
	v_exp_f32_e32 v149, v149
	v_and_b32_e32 v153, 0xffff0000, v194
	v_fmac_f32_e32 v153, v151, v147
	v_and_b32_e32 v147, 0xffff0000, v195
	v_fmac_f32_e32 v147, v145, v149
	v_cvt_pk_bf16_f32 v194, v153, v147
	ds_read_b64 v[196:197], v189 offset:1792
	s_waitcnt lgkmcnt(0)
	v_lshlrev_b32_e32 v145, 16, v196
	v_lshlrev_b32_e32 v149, 16, v197
	v_exp_f32_e32 v145, v145
	v_exp_f32_e32 v149, v149
	v_and_b32_e32 v151, 0xffff0000, v196
	v_fmac_f32_e32 v151, v153, v145
	v_and_b32_e32 v145, 0xffff0000, v197
	v_fmac_f32_e32 v145, v147, v149
	v_cvt_pk_bf16_f32 v196, v151, v145
	ds_read_b64 v[198:199], v189 offset:1920
	s_waitcnt lgkmcnt(0)
	v_lshlrev_b32_e32 v147, 16, v198
	v_lshlrev_b32_e32 v149, 16, v199
	v_exp_f32_e32 v147, v147
	v_exp_f32_e32 v149, v149
	v_and_b32_e32 v153, 0xffff0000, v198
	v_fmac_f32_e32 v153, v151, v147
	v_and_b32_e32 v147, 0xffff0000, v199
	v_fmac_f32_e32 v147, v145, v149
	v_cvt_pk_bf16_f32 v198, v153, v147
	ds_read_b64 v[200:201], v189 offset:2048
	s_waitcnt lgkmcnt(0)
	v_lshlrev_b32_e32 v145, 16, v200
	v_lshlrev_b32_e32 v149, 16, v201
	v_exp_f32_e32 v145, v145
	v_exp_f32_e32 v149, v149
	v_and_b32_e32 v151, 0xffff0000, v200
	v_fmac_f32_e32 v151, v153, v145
	v_and_b32_e32 v145, 0xffff0000, v201
	v_fmac_f32_e32 v145, v147, v149
	v_cvt_pk_bf16_f32 v201, v151, v145
	ds_read_b64 v[202:203], v189 offset:2176
	s_waitcnt lgkmcnt(0)
	v_lshlrev_b32_e32 v147, 16, v202
	v_lshlrev_b32_e32 v149, 16, v203
	v_exp_f32_e32 v147, v147
	v_exp_f32_e32 v149, v149
	v_and_b32_e32 v153, 0xffff0000, v202
	v_fmac_f32_e32 v153, v151, v147
	v_and_b32_e32 v147, 0xffff0000, v203
	v_fmac_f32_e32 v147, v145, v149
	v_cvt_pk_bf16_f32 v203, v153, v147
	ds_read_b64 v[204:205], v189 offset:2304
	s_waitcnt lgkmcnt(0)
	v_lshlrev_b32_e32 v145, 16, v204
	v_lshlrev_b32_e32 v149, 16, v205
	v_exp_f32_e32 v145, v145
	v_exp_f32_e32 v149, v149
	v_and_b32_e32 v151, 0xffff0000, v204
	v_fmac_f32_e32 v151, v153, v145
	v_and_b32_e32 v145, 0xffff0000, v205
	v_fmac_f32_e32 v145, v147, v149
	v_cvt_pk_bf16_f32 v205, v151, v145
	ds_read_b64 v[206:207], v189 offset:2432
	s_waitcnt lgkmcnt(0)
	v_lshlrev_b32_e32 v147, 16, v206
	v_lshlrev_b32_e32 v149, 16, v207
	v_exp_f32_e32 v147, v147
	v_exp_f32_e32 v149, v149
	v_and_b32_e32 v153, 0xffff0000, v206
	v_fmac_f32_e32 v153, v151, v147
	v_and_b32_e32 v147, 0xffff0000, v207
	v_fmac_f32_e32 v147, v145, v149
	v_cvt_pk_bf16_f32 v207, v153, v147
	ds_read_b64 v[208:209], v189 offset:2560
	s_waitcnt lgkmcnt(0)
	v_lshlrev_b32_e32 v145, 16, v208
	v_lshlrev_b32_e32 v149, 16, v209
	v_exp_f32_e32 v145, v145
	v_exp_f32_e32 v149, v149
	v_and_b32_e32 v151, 0xffff0000, v208
	v_fmac_f32_e32 v151, v153, v145
	v_and_b32_e32 v145, 0xffff0000, v209
	v_fmac_f32_e32 v145, v147, v149
	v_cvt_pk_bf16_f32 v209, v151, v145
	ds_read_b64 v[210:211], v189 offset:2688
	s_waitcnt lgkmcnt(0)
	v_lshlrev_b32_e32 v147, 16, v210
	v_lshlrev_b32_e32 v149, 16, v211
	v_exp_f32_e32 v147, v147
	v_exp_f32_e32 v149, v149
	v_and_b32_e32 v153, 0xffff0000, v210
	v_fmac_f32_e32 v153, v151, v147
	v_and_b32_e32 v147, 0xffff0000, v211
	v_fmac_f32_e32 v147, v145, v149
	v_cvt_pk_bf16_f32 v211, v153, v147
	ds_read_b64 v[212:213], v189 offset:2816
	s_waitcnt lgkmcnt(0)
	v_lshlrev_b32_e32 v145, 16, v212
	v_lshlrev_b32_e32 v149, 16, v213
	v_exp_f32_e32 v145, v145
	v_exp_f32_e32 v149, v149
	v_and_b32_e32 v151, 0xffff0000, v212
	v_fmac_f32_e32 v151, v153, v145
	v_and_b32_e32 v145, 0xffff0000, v213
	v_fmac_f32_e32 v145, v147, v149
	v_cvt_pk_bf16_f32 v214, v151, v145
	ds_read_b64 v[212:213], v189 offset:2944
	s_waitcnt lgkmcnt(0)
	v_lshlrev_b32_e32 v147, 16, v212
	v_lshlrev_b32_e32 v149, 16, v213
	v_exp_f32_e32 v147, v147
	v_exp_f32_e32 v149, v149
	v_and_b32_e32 v153, 0xffff0000, v212
	v_fmac_f32_e32 v153, v151, v147
	v_and_b32_e32 v147, 0xffff0000, v213
	v_fmac_f32_e32 v147, v145, v149
	v_cvt_pk_bf16_f32 v216, v153, v147
	ds_read_b64 v[212:213], v189 offset:3072
	s_waitcnt lgkmcnt(0)
	v_lshlrev_b32_e32 v145, 16, v212
	v_lshlrev_b32_e32 v149, 16, v213
	v_exp_f32_e32 v145, v145
	v_exp_f32_e32 v149, v149
	v_and_b32_e32 v151, 0xffff0000, v212
	v_fmac_f32_e32 v151, v153, v145
	v_and_b32_e32 v145, 0xffff0000, v213
	v_fmac_f32_e32 v145, v147, v149
	v_cvt_pk_bf16_f32 v218, v151, v145
	ds_read_b64 v[212:213], v189 offset:3200
	s_waitcnt lgkmcnt(0)
	v_lshlrev_b32_e32 v147, 16, v212
	v_lshlrev_b32_e32 v149, 16, v213
	v_exp_f32_e32 v147, v147
	v_exp_f32_e32 v149, v149
	v_and_b32_e32 v153, 0xffff0000, v212
	v_fmac_f32_e32 v153, v151, v147
	v_and_b32_e32 v147, 0xffff0000, v213
	v_fmac_f32_e32 v147, v145, v149
	v_cvt_pk_bf16_f32 v220, v153, v147
	ds_read_b64 v[212:213], v189 offset:3328
	s_waitcnt lgkmcnt(0)
	v_lshlrev_b32_e32 v145, 16, v212
	v_lshlrev_b32_e32 v149, 16, v213
	v_exp_f32_e32 v145, v145
	v_exp_f32_e32 v149, v149
	v_and_b32_e32 v151, 0xffff0000, v212
	v_fmac_f32_e32 v151, v153, v145
	v_and_b32_e32 v145, 0xffff0000, v213
	v_fmac_f32_e32 v145, v147, v149
	v_cvt_pk_bf16_f32 v222, v151, v145
	ds_read_b64 v[212:213], v189 offset:3456
	s_waitcnt lgkmcnt(0)
	v_lshlrev_b32_e32 v147, 16, v212
	v_lshlrev_b32_e32 v149, 16, v213
	v_exp_f32_e32 v147, v147
	v_exp_f32_e32 v149, v149
	v_and_b32_e32 v153, 0xffff0000, v212
	v_fmac_f32_e32 v153, v151, v147
	v_and_b32_e32 v147, 0xffff0000, v213
	v_fmac_f32_e32 v147, v145, v149
	v_cvt_pk_bf16_f32 v225, v153, v147
	ds_read_b64 v[212:213], v189 offset:3584
	s_waitcnt lgkmcnt(0)
	v_lshlrev_b32_e32 v145, 16, v212
	v_lshlrev_b32_e32 v149, 16, v213
	v_exp_f32_e32 v145, v145
	v_exp_f32_e32 v149, v149
	v_and_b32_e32 v151, 0xffff0000, v212
	v_fmac_f32_e32 v151, v153, v145
	v_and_b32_e32 v145, 0xffff0000, v213
	v_fmac_f32_e32 v145, v147, v149
	v_cvt_pk_bf16_f32 v227, v151, v145
	ds_read_b64 v[212:213], v189 offset:3712
	s_waitcnt lgkmcnt(0)
	v_lshlrev_b32_e32 v147, 16, v212
	v_lshlrev_b32_e32 v149, 16, v213
	v_exp_f32_e32 v147, v147
	v_exp_f32_e32 v149, v149
	v_and_b32_e32 v153, 0xffff0000, v212
	v_fmac_f32_e32 v153, v151, v147
	v_and_b32_e32 v147, 0xffff0000, v213
	v_fmac_f32_e32 v147, v145, v149
	v_cvt_pk_bf16_f32 v229, v153, v147
	ds_read_b64 v[212:213], v189 offset:3840
	s_waitcnt lgkmcnt(0)
	v_lshlrev_b32_e32 v145, 16, v212
	v_lshlrev_b32_e32 v149, 16, v213
	v_exp_f32_e32 v145, v145
	v_exp_f32_e32 v149, v149
	v_and_b32_e32 v151, 0xffff0000, v212
	v_fmac_f32_e32 v151, v153, v145
	v_and_b32_e32 v145, 0xffff0000, v213
	v_fmac_f32_e32 v145, v147, v149
	v_cvt_pk_bf16_f32 v231, v151, v145
	ds_read_b64 v[212:213], v189 offset:3968
	s_waitcnt lgkmcnt(0)
	v_lshlrev_b32_e32 v147, 16, v212
	v_lshlrev_b32_e32 v149, 16, v213
	v_exp_f32_e32 v147, v147
	v_exp_f32_e32 v149, v149
	v_and_b32_e32 v153, 0xffff0000, v212
	v_fmac_f32_e32 v153, v151, v147
	v_and_b32_e32 v147, 0xffff0000, v213
	v_fmac_f32_e32 v147, v145, v149
	v_or_b32_e32 v145, s44, v68
	v_mov_b64_e32 v[212:213], s[12:13]
	v_mad_u64_u32 v[212:213], s[46:47], v145, s3, v[212:213]
	v_mad_i32_i24 v213, s45, v169, v213
	v_lshl_add_u64 v[100:101], v[100:101], 1, v[212:213]
	v_subrev_u32_e32 v243, s12, v100
	v_cvt_pk_bf16_f32 v233, v153, v147
	global_load_dword v145, v243, s[12:13]
	v_add_u32_e32 v243, 0x1400, v243
	global_load_dword v147, v243, s[12:13]
	v_add_u32_e32 v243, 0x1400, v243
	global_load_dword v149, v243, s[12:13]
	v_add_u32_e32 v243, 0x1400, v243
	global_load_dword v151, v243, s[12:13]
	v_add_u32_e32 v243, 0x1400, v243
	global_load_dword v153, v243, s[12:13]
	v_add_u32_e32 v243, 0x1400, v243
	global_load_dword v154, v243, s[12:13]
	v_add_u32_e32 v243, 0x1400, v243
	global_load_dword v156, v243, s[12:13]
	v_add_u32_e32 v243, 0x1400, v243
	global_load_dword v193, v243, s[12:13]
	v_add_u32_e32 v243, 0x1400, v243
	global_load_dword v195, v243, s[12:13]
	v_add_u32_e32 v243, 0x1400, v243
	global_load_dword v197, v243, s[12:13]
	v_add_u32_e32 v243, 0x1400, v243
	global_load_dword v199, v243, s[12:13]
	v_add_u32_e32 v243, 0x1400, v243
	global_load_dword v200, v243, s[12:13]
	v_add_u32_e32 v243, 0x1400, v243
	global_load_dword v202, v243, s[12:13]
	v_add_u32_e32 v243, 0x1400, v243
	global_load_dword v204, v243, s[12:13]
	v_add_u32_e32 v243, 0x1400, v243
	global_load_dword v206, v243, s[12:13]
	v_add_u32_e32 v243, 0x1400, v243
	global_load_dword v208, v243, s[12:13]
	v_add_u32_e32 v243, 0x1400, v243
	global_load_dword v210, v243, s[12:13]
	v_add_u32_e32 v243, 0x1400, v243
	global_load_dword v212, v243, s[12:13]
	v_add_u32_e32 v243, 0x1400, v243
	global_load_dword v213, v243, s[12:13]
	v_add_u32_e32 v243, 0x1400, v243
	global_load_dword v215, v243, s[12:13]
	v_add_u32_e32 v243, 0x1400, v243
	global_load_dword v217, v243, s[12:13]
	v_add_u32_e32 v243, 0x1400, v243
	global_load_dword v219, v243, s[12:13]
	v_add_u32_e32 v243, 0x1400, v243
	global_load_dword v221, v243, s[12:13]
	v_add_u32_e32 v243, 0x1400, v243
	global_load_dword v223, v243, s[12:13]
	v_add_u32_e32 v243, 0x1400, v243
	global_load_dword v224, v243, s[12:13]
	v_add_u32_e32 v243, 0x1400, v243
	global_load_dword v226, v243, s[12:13]
	v_add_u32_e32 v243, 0x1400, v243
	global_load_dword v228, v243, s[12:13]
	v_add_u32_e32 v243, 0x1400, v243
	global_load_dword v230, v243, s[12:13]
	v_add_u32_e32 v243, 0x1400, v243
	global_load_dword v232, v243, s[12:13]
	v_add_u32_e32 v243, 0x1400, v243
	global_load_dword v234, v243, s[12:13]
	v_add_u32_e32 v243, 0x1400, v243
	global_load_dword v235, v243, s[12:13]
	v_add_u32_e32 v243, 0x1400, v243
	global_load_dword v236, v243, s[12:13]
	s_waitcnt vmcnt(32)
	v_pk_fma_f32 v[100:101], v[102:103], 0, v[106:107] op_sel_hi:[1,0,1]
	v_pk_mul_f32 v[102:103], v[102:103], v[110:111]
	v_pk_fma_f32 v[100:101], v[100:101], v[110:111], v[104:105]
	v_pk_mul_f32 v[102:103], v[102:103], v[108:109]
	v_pk_fma_f32 v[100:101], v[100:101], v[108:109], v[114:115]
	v_pk_mul_f32 v[102:103], v[102:103], v[118:119]
	v_pk_fma_f32 v[100:101], v[100:101], v[118:119], v[112:113]
	v_pk_mul_f32 v[102:103], v[102:103], v[116:117]
	v_pk_fma_f32 v[100:101], v[100:101], v[116:117], v[122:123]
	v_pk_mul_f32 v[102:103], v[102:103], v[126:127]
	v_pk_fma_f32 v[100:101], v[100:101], v[126:127], v[120:121]
	v_pk_mul_f32 v[102:103], v[102:103], v[124:125]
	v_pk_fma_f32 v[100:101], v[100:101], v[124:125], v[130:131]
	v_pk_mul_f32 v[102:103], v[102:103], v[134:135]
	v_pk_fma_f32 v[100:101], v[100:101], v[134:135], v[128:129]
	v_pk_mul_f32 v[108:109], v[102:103], v[132:133]
	v_pk_fma_f32 v[110:111], v[100:101], v[132:133], v[136:137]
	ds_bpermute_b32 v112, v73, v108
	ds_bpermute_b32 v113, v73, v109
	ds_bpermute_b32 v114, v73, v110
	ds_bpermute_b32 v115, v73, v111
	ds_bpermute_b32 v100, v166, v108
	ds_bpermute_b32 v101, v166, v109
	ds_bpermute_b32 v102, v166, v110
	ds_bpermute_b32 v103, v166, v111
	ds_bpermute_b32 v104, v167, v108
	ds_bpermute_b32 v105, v167, v109
	ds_bpermute_b32 v106, v167, v110
	ds_bpermute_b32 v107, v167, v111
	ds_bpermute_b32 v108, v168, v108
	ds_bpermute_b32 v109, v168, v109
	ds_bpermute_b32 v110, v168, v110
	ds_bpermute_b32 v111, v168, v111
	s_cselect_b64 s[46:47], -1, 0
	s_and_b64 vcc, exec, s[46:47]
	ds_write_b128 v173, v[22:25]
	ds_write_b128 v174, v[2:5]
	ds_write_b128 v175, v[6:9]
	ds_write_b128 v176, v[10:13]
	ds_write_b128 v177, v[14:17] offset:128
	ds_write_b128 v178, v[18:21] offset:128
	ds_write_b128 v179, v[26:29] offset:128
	ds_write_b128 v180, v[30:33] offset:128
	ds_write_b128 v181, v[34:37] offset:256
	ds_write_b128 v182, v[38:41] offset:256
	ds_write_b128 v183, v[42:45] offset:256
	ds_write_b128 v184, v[46:49] offset:256
	ds_write_b128 v185, v[50:53] offset:384
	ds_write_b128 v186, v[54:57] offset:384
	ds_write_b128 v187, v[58:61] offset:384
	ds_write_b128 v188, v[62:65] offset:384
	s_cbranch_vccnz .Lp9_nonext
	s_ashr_i32 s48, s53, 2
	s_ashr_i32 s49, s48, 31
	s_lshl_b64 s[48:49], s[48:49], 17
	s_add_u32 s43, s29, s48
	s_addc_u32 s49, s30, s49
	s_and_b32 s48, s34, 0xc000
	s_add_u32 s48, s43, s48
	s_addc_u32 s49, s49, 0
	global_load_dwordx4 v[22:25], v66, s[48:49] nt
	global_load_dwordx4 v[2:5], v66, s[48:49] offset:1024 nt
	global_load_dwordx4 v[6:9], v66, s[48:49] offset:2048 nt
	s_nop 0
	global_load_dwordx4 v[10:13], v66, s[48:49] offset:3072 nt
	global_load_dwordx4 v[14:17], v74, s[48:49] nt
	s_nop 0
	global_load_dwordx4 v[18:21], v76, s[48:49] nt
	s_nop 0
	global_load_dwordx4 v[26:29], v78, s[48:49] nt
	s_nop 0
	global_load_dwordx4 v[30:33], v80, s[48:49] nt
	s_nop 0
	global_load_dwordx4 v[34:37], v82, s[48:49] nt
	s_nop 0
	global_load_dwordx4 v[38:41], v84, s[48:49] nt
	s_nop 0
	global_load_dwordx4 v[42:45], v86, s[48:49] nt
	s_nop 0
	global_load_dwordx4 v[46:49], v88, s[48:49] nt
	s_nop 0
	global_load_dwordx4 v[50:53], v90, s[48:49] nt
	s_nop 0
	global_load_dwordx4 v[54:57], v92, s[48:49] nt
	s_nop 0
	global_load_dwordx4 v[58:61], v94, s[48:49] nt
	s_nop 0
	global_load_dwordx4 v[62:65], v96, s[48:49] nt
	s_branch .LBB0_1466
